# v042 + grid barrier: round index from a per-workgroup counter instead of dividing the arrival ticket; leader forms release addresses while its write-back is in flight
# speedup vs baseline: 1.0089x; 1.0055x over previous
; #define LAS __attribute__((address_space(3)))
; __global__ void __launch_bounds__(NTHR, 2) mk_fwd(Args args) {
;     extern __shared__ __attribute__((aligned(16))) unsigned char lds_raw[];
;     LAS unsigned char* lds = (LAS unsigned char*)lds_raw;
;     const int G = gridDim.x;
;     const int vcu = (G % 8 == 0) ? ((int)blockIdx.x % 8) * (G / 8) + (int)blockIdx.x / 8 : (int)blockIdx.x;
;     volatile LAS unsigned* MISC = (volatile LAS unsigned*)(lds + LDS_MISC);
;     LAS int* blkoff = (LAS int*)(lds + LDS_TBL);
;     if (threadIdx.x < 4) MISC[threadIdx.x] = 0u;
;     __syncthreads();
_Z6mk_fwd4Args:
	s_mov_b64 s[76:77], s[0:1]
	s_load_dword s68, s[0:1], 0xf0
	s_nop 0
	s_load_dwordx2 s[0:1], s[0:1], 0xd8
	s_nop 0
	s_load_dwordx4 s[56:59], s[76:77], 0xe0
	s_add_u32 s4, s76, 0xf0
	s_addc_u32 s5, s77, 0
	s_waitcnt lgkmcnt(0)
	s_and_b32 s3, s68, 7
	v_writelane_b32 v253, s4, 0
	s_cmp_lg_u32 s3, 0
	s_mov_b32 s86, s2
	s_mov_b32 s8, 2
	s_nop 0
	v_writelane_b32 v255, s8, 61
	v_writelane_b32 v253, s5, 1
	s_cbranch_scc0 .LBB0_117
	v_cmp_gt_u32_e32 vcc, 4, v0
	s_and_saveexec_b64 s[4:5], vcc

; __device__ __forceinline__ unsigned xb_ld(unsigned* p)              { return __hip_atomic_load(p, __ATOMIC_RELAXED, __HIP_MEMORY_SCOPE_AGENT); }
; __device__ __forceinline__ unsigned xb_add(unsigned* p, unsigned v) { return __hip_atomic_fetch_add(p, v, __ATOMIC_RELAXED, __HIP_MEMORY_SCOPE_AGENT); }
; #define XB_SPIN(cond, bar) do { unsigned _sp = 0; while (cond) { __builtin_amdgcn_s_sleep(1); \
;     if ((++_sp & 255u) == 0u) { if (xb_ld(&(bar)[XB_TMO])) break; if (_sp > XB_SPIN_CAP) { atomicAdd(&(bar)[XB_TMO], 1u); break; } } } } while (0)
; __device__ __forceinline__ void xcd_barrier(const XcdBarrier& b) {
;     ...
;         const unsigned old = xb_add(&bar[XB_XSUB(b.x)], 1u);
;         const unsigned gen = old / nloc;
;         if (old + 1u == (gen + 1u) * nloc) {
;             __builtin_amdgcn_fence(__ATOMIC_RELEASE, "agent");
;             asm volatile("s_waitcnt vmcnt(0)" ::: "memory");
;             const unsigned og = xb_add(&bar[XB_TOP], 1u);
;             const unsigned tg = og / nx;
;             if (og + 1u == (tg + 1u) * nx) xb_add(&bar[XB_TOPGEN], 1u);
;             else XB_SPIN(xb_ld(&bar[XB_TOPGEN]) == tg, bar);
;             __builtin_amdgcn_fence(__ATOMIC_ACQUIRE, "agent");
;             xb_add(&bar[XB_XGEN(b.x)], 1u);
;             asm volatile("s_waitcnt vmcnt(0)" ::: "memory");
;         } else {
;             XB_SPIN(xb_ld(&bar[XB_XGEN(b.x)]) == gen, bar);
.LBB0_301:
	s_or_b64 exec, exec, s[6:7]
	v_readlane_b32 s12, v255, 61
	s_waitcnt lgkmcnt(0)
	s_add_i32 s13, s12, 1
	v_mul_lo_u32 v3, v3, s13
	v_mov_b32_e32 v1, s12
	v_writelane_b32 v255, s13, 61
	s_waitcnt vmcnt(0)
	buffer_inv sc1
	v_readfirstlane_b32 s5, v4
	s_add_i32 s5, s5, 1
	v_mov_b32_e32 v4, s5
	v_cmp_ne_u32_e32 vcc, v4, v3
	s_waitcnt lgkmcnt(0)
	v_add_u32_e32 v16, -1, v1
	v_mul_lo_u32 v16, v16, v2
	s_and_saveexec_b64 s[6:7], vcc
	s_xor_b64 s[6:7], exec, s[6:7]
	s_cbranch_execz .LBB0_315
	v_readlane_b32 s8, v253, 48
	v_readlane_b32 s9, v253, 49
	s_waitcnt lgkmcnt(0)
	s_nop 3
	s_add_u32 s8, s8, 0x3600
	s_addc_u32 s9, s9, 0
	s_mov_b32 s20, 0
	global_load_dword v2, v163, s[8:9] sc1
	s_sleep 10

; __device__ __forceinline__ unsigned xb_ld(unsigned* p)              { return __hip_atomic_load(p, __ATOMIC_RELAXED, __HIP_MEMORY_SCOPE_AGENT); }
; __device__ __forceinline__ unsigned xb_add(unsigned* p, unsigned v) { return __hip_atomic_fetch_add(p, v, __ATOMIC_RELAXED, __HIP_MEMORY_SCOPE_AGENT); }
; #define XB_SPIN(cond, bar) do { unsigned _sp = 0; while (cond) { __builtin_amdgcn_s_sleep(1); \
;     if ((++_sp & 255u) == 0u) { if (xb_ld(&(bar)[XB_TMO])) break; if (_sp > XB_SPIN_CAP) { atomicAdd(&(bar)[XB_TMO], 1u); break; } } } } while (0)
; __device__ __forceinline__ void xcd_barrier(const XcdBarrier& b) {
;     ...
;         if (old + 1u == (gen + 1u) * nloc) {
;             __builtin_amdgcn_fence(__ATOMIC_RELEASE, "agent");
;             asm volatile("s_waitcnt vmcnt(0)" ::: "memory");
;             const unsigned og = xb_add(&bar[XB_TOP], 1u);
;             const unsigned tg = og / nx;
;             if (og + 1u == (tg + 1u) * nx) xb_add(&bar[XB_TOPGEN], 1u);
;             else XB_SPIN(xb_ld(&bar[XB_TOPGEN]) == tg, bar);
;             __builtin_amdgcn_fence(__ATOMIC_ACQUIRE, "agent");
;             xb_add(&bar[XB_XGEN(b.x)], 1u);
.LBB0_315:
	s_andn2_saveexec_b64 s[6:7], s[6:7]
	s_cbranch_execz .LBB0_335
	s_mov_b64 s[6:7], exec
	buffer_wbl2 sc1
	v_readlane_b32 s18, v253, 48
	v_readlane_b32 s19, v253, 49
	v_readlane_b32 s12, v253, 52
	v_readlane_b32 s13, v253, 53
	s_nop 3
	s_add_u32 s18, s18, 0x3600
	s_addc_u32 s19, s19, 0
	s_add_u32 s12, s12, 0x2500
	s_addc_u32 s13, s13, 0
	s_waitcnt lgkmcnt(0)
	s_waitcnt vmcnt(0)
	global_atomic_add v163, v197, s[12:13]
	global_atomic_add v163, v197, s[12:13] offset:256
	global_atomic_add v163, v197, s[12:13] offset:512
	global_atomic_add v163, v197, s[12:13] offset:768
	global_atomic_add v163, v197, s[12:13] offset:1024
	global_atomic_add v163, v197, s[12:13] offset:1280
	global_atomic_add v163, v197, s[12:13] offset:1536
	global_atomic_add v163, v197, s[12:13] offset:1792
	global_atomic_add v163, v197, s[12:13] offset:2048
	global_atomic_add v163, v197, s[12:13] offset:2304
	global_atomic_add v163, v197, s[12:13] offset:2560
	global_atomic_add v163, v197, s[12:13] offset:2816
	global_atomic_add v163, v197, s[12:13] offset:3072
	global_atomic_add v163, v197, s[12:13] offset:3328
	global_atomic_add v163, v197, s[12:13] offset:3584
	global_atomic_add v163, v197, s[12:13] offset:3840
	s_mov_b32 s5, 0

; __device__ __forceinline__ unsigned xb_ld(unsigned* p)              { return __hip_atomic_load(p, __ATOMIC_RELAXED, __HIP_MEMORY_SCOPE_AGENT); }
; __device__ __forceinline__ unsigned xb_add(unsigned* p, unsigned v) { return __hip_atomic_fetch_add(p, v, __ATOMIC_RELAXED, __HIP_MEMORY_SCOPE_AGENT); }
; #define XB_SPIN(cond, bar) do { unsigned _sp = 0; while (cond) { __builtin_amdgcn_s_sleep(1); \
;     if ((++_sp & 255u) == 0u) { if (xb_ld(&(bar)[XB_TMO])) break; if (_sp > XB_SPIN_CAP) { atomicAdd(&(bar)[XB_TMO], 1u); break; } } } } while (0)
; __device__ __forceinline__ void xcd_barrier(const XcdBarrier& b) {
;     ...
;         const unsigned old = xb_add(&bar[XB_XSUB(b.x)], 1u);
;         const unsigned gen = old / nloc;
;         if (old + 1u == (gen + 1u) * nloc) {
;             __builtin_amdgcn_fence(__ATOMIC_RELEASE, "agent");
;             asm volatile("s_waitcnt vmcnt(0)" ::: "memory");
;             const unsigned og = xb_add(&bar[XB_TOP], 1u);
;             const unsigned tg = og / nx;
;             if (og + 1u == (tg + 1u) * nx) xb_add(&bar[XB_TOPGEN], 1u);
;             else XB_SPIN(xb_ld(&bar[XB_TOPGEN]) == tg, bar);
;             __builtin_amdgcn_fence(__ATOMIC_ACQUIRE, "agent");
;             xb_add(&bar[XB_XGEN(b.x)], 1u);
;             asm volatile("s_waitcnt vmcnt(0)" ::: "memory");
;         } else {
;             XB_SPIN(xb_ld(&bar[XB_XGEN(b.x)]) == gen, bar);
.LBB0_1538:
	s_or_b64 exec, exec, s[6:7]
	v_readlane_b32 s12, v255, 61
	s_waitcnt lgkmcnt(0)
	s_add_i32 s13, s12, 1
	v_mul_lo_u32 v3, v3, s13
	v_mov_b32_e32 v1, s12
	v_writelane_b32 v255, s13, 61
	s_waitcnt vmcnt(0)
	buffer_inv sc1
	v_readfirstlane_b32 s4, v4
	s_add_i32 s4, s4, 1
	v_mov_b32_e32 v4, s4
	v_cmp_ne_u32_e32 vcc, v4, v3
	s_waitcnt lgkmcnt(0)
	v_add_u32_e32 v16, -1, v1
	v_mul_lo_u32 v16, v16, v2
	s_and_saveexec_b64 s[4:5], vcc
	s_xor_b64 s[6:7], exec, s[4:5]
	s_cbranch_execz .LBB0_1552
	v_readlane_b32 s8, v253, 48
	v_readlane_b32 s9, v253, 49
	s_waitcnt lgkmcnt(0)
	s_nop 3
	s_add_u32 s8, s8, 0x3600
	s_addc_u32 s9, s9, 0
	s_mov_b32 s20, 0
	global_load_dword v2, v163, s[8:9] sc1
	s_sleep 10

; __device__ __forceinline__ unsigned xb_ld(unsigned* p)              { return __hip_atomic_load(p, __ATOMIC_RELAXED, __HIP_MEMORY_SCOPE_AGENT); }
; __device__ __forceinline__ unsigned xb_add(unsigned* p, unsigned v) { return __hip_atomic_fetch_add(p, v, __ATOMIC_RELAXED, __HIP_MEMORY_SCOPE_AGENT); }
; #define XB_SPIN(cond, bar) do { unsigned _sp = 0; while (cond) { __builtin_amdgcn_s_sleep(1); \
;     if ((++_sp & 255u) == 0u) { if (xb_ld(&(bar)[XB_TMO])) break; if (_sp > XB_SPIN_CAP) { atomicAdd(&(bar)[XB_TMO], 1u); break; } } } } while (0)
; __device__ __forceinline__ void xcd_barrier(const XcdBarrier& b) {
;     ...
;         if (old + 1u == (gen + 1u) * nloc) {
;             __builtin_amdgcn_fence(__ATOMIC_RELEASE, "agent");
;             asm volatile("s_waitcnt vmcnt(0)" ::: "memory");
;             const unsigned og = xb_add(&bar[XB_TOP], 1u);
;             const unsigned tg = og / nx;
;             if (og + 1u == (tg + 1u) * nx) xb_add(&bar[XB_TOPGEN], 1u);
;             else XB_SPIN(xb_ld(&bar[XB_TOPGEN]) == tg, bar);
;             __builtin_amdgcn_fence(__ATOMIC_ACQUIRE, "agent");
;             xb_add(&bar[XB_XGEN(b.x)], 1u);
.LBB0_1553:
	s_mov_b64 s[6:7], exec
	buffer_wbl2 sc1
	v_readlane_b32 s18, v253, 48
	v_readlane_b32 s19, v253, 49
	v_readlane_b32 s12, v253, 52
	v_readlane_b32 s13, v253, 53
	s_nop 3
	s_add_u32 s18, s18, 0x3600
	s_addc_u32 s19, s19, 0
	s_add_u32 s12, s12, 0x2500
	s_addc_u32 s13, s13, 0
	s_waitcnt lgkmcnt(0)
	s_waitcnt vmcnt(0)
	global_atomic_add v163, v197, s[12:13]
	global_atomic_add v163, v197, s[12:13] offset:256
	global_atomic_add v163, v197, s[12:13] offset:512
	global_atomic_add v163, v197, s[12:13] offset:768
	global_atomic_add v163, v197, s[12:13] offset:1024
	global_atomic_add v163, v197, s[12:13] offset:1280
	global_atomic_add v163, v197, s[12:13] offset:1536
	global_atomic_add v163, v197, s[12:13] offset:1792
	global_atomic_add v163, v197, s[12:13] offset:2048
	global_atomic_add v163, v197, s[12:13] offset:2304
	global_atomic_add v163, v197, s[12:13] offset:2560
	global_atomic_add v163, v197, s[12:13] offset:2816
	global_atomic_add v163, v197, s[12:13] offset:3072
	global_atomic_add v163, v197, s[12:13] offset:3328
	global_atomic_add v163, v197, s[12:13] offset:3584
	global_atomic_add v163, v197, s[12:13] offset:3840
	s_mov_b32 s5, 0
